# layer-0 projection: the 64 workgroups that run a ninth gate unit skip the split-K context tasks, the other 192 share them
# speedup vs baseline: 1.0050x; 1.0001x over previous
.LBB0_460:
	s_cmp_lt_u32 s2, 64
	s_cbranch_scc1 .LBB0_466
	v_and_b32_e32 v4, 15, v0
	v_lshlrev_b32_e32 v1, 8, v0
	v_and_b32_e32 v1, 0x1c000, v1
	s_waitcnt vmcnt(0)
	v_lshlrev_b32_e32 v3, 8, v4
	v_bfe_u32 v2, v0, 4, 2
	v_add3_u32 v7, 0, v1, v3
	v_lshlrev_b32_e32 v3, 3, v0
	v_mov_b32_e32 v67, 0
	v_lshlrev_b32_e32 v8, 5, v2
	v_lshrrev_b32_e32 v1, 3, v0
	v_and_b32_e32 v88, 56, v3
	v_lshlrev_b32_e32 v66, 4, v2
	v_and_b32_e32 v2, 0xe00, v3
	v_mov_b32_e32 v3, v67
	v_lshlrev_b32_e32 v5, 1, v0
	v_and_b32_e32 v6, 3, v0
	v_lshlrev_b32_e32 v9, 8, v1
	v_lshlrev_b32_e32 v10, 2, v88
	v_lshl_add_u64 v[2:3], s[40:41], 0, v[2:3]
	s_mov_b64 s[4:5], 0x800080
	v_add3_u32 v89, 0, v9, v10
	v_lshl_add_u64 v[68:69], v[2:3], 0, s[4:5]
	v_and_or_b32 v98, v5, 24, v6
	s_mov_b64 s[4:5], 0x2a000080
	v_add_u32_e32 v90, 0x10000, v89
	v_add_u32_e32 v91, 0x10010, v89
	v_add_u32_e32 v92, 0x14000, v89
	v_add_u32_e32 v93, 0x14010, v89
	v_add_u32_e32 v94, 0x18000, v89
	v_add_u32_e32 v95, 0x18010, v89
	v_add_u32_e32 v96, 0x1c000, v89
	v_add_u32_e32 v97, 0x1c010, v89
	v_or_b32_e32 v99, 36, v98
	v_lshl_add_u64 v[70:71], v[2:3], 0, s[4:5]
	v_or_b32_e32 v100, 0x4000, v4
	v_or_b32_e32 v101, 32, v98
	v_or_b32_e32 v102, 4, v98
	v_or_b32_e32 v103, 0x4010, v4
	v_or_b32_e32 v104, 0x4030, v4
	v_or_b32_e32 v105, 0x4020, v4
	s_mov_b64 s[4:5], 0x100
	v_add_u32_e32 v106, v7, v8
	s_waitcnt lgkmcnt(0)
	s_movk_i32 s8, 0x2100
	s_add_i32 s9, s2, 0xffffffc0
	s_branch .LBB0_462
.LBB0_461:
	s_addk_i32 s10, 0x4000
	v_add_u32_e32 v15, s10, v1
	v_lshl_or_b32 v14, s11, 6, v88
	v_cvt_pk_bf16_f32 v11, v2, v3
	v_mov_b64_e32 v[2:3], s[6:7]
	v_mad_i64_i32 v[2:3], s[10:11], v15, s8, v[2:3]
	v_ashrrev_i32_e32 v15, 31, v14
	s_add_i32 s9, s9, s30
	s_sub_i32 s9, s9, 64
	v_cvt_pk_bf16_f32 v10, v4, v5
	v_cvt_pk_bf16_f32 v12, v8, v9
	v_cvt_pk_bf16_f32 v13, v6, v7
	v_lshl_add_u64 v[2:3], v[14:15], 1, v[2:3]
	s_cmpk_lt_i32 s9, 0x200
	global_store_dwordx4 v[2:3], v[10:13], off
	s_cbranch_scc0 .LBB0_466
